# router phase carries a second W1-conversion slice in groups 0..3 (experts 12,13 staged in spare VGPRs); stand-alone conversion stage skips those experts on the 256-WG grid
# speedup vs baseline: 1.0076x; 1.0076x over previous
.LBB0_215:
	s_cmp_lt_i32 s4, 3
	s_waitcnt lgkmcnt(0)
	s_cselect_b64 s[0:1], -1, 0
	s_cmp_gt_i32 s5, 2
	s_cselect_b64 s[2:3], -1, 0
	s_and_b64 s[0:1], s[0:1], s[2:3]
	s_andn2_b64 vcc, exec, s[0:1]
	s_cbranch_vccnz .LBB0_347
	v_readlane_b32 s18, v254, 11
	s_load_dword s6, s[52:53], 0xd0
	s_load_dwordx2 s[4:5], s[52:53], 0xc0
	s_bitcmp0_b32 s18, 0
	s_cselect_b64 s[0:1], -1, 0
	s_bitcmp1_b32 s18, 0
	v_readlane_b32 s8, v254, 10
	s_cselect_b64 s[10:11], -1, 0
	s_lshl_b32 s2, s8, 14
	s_add_i32 s36, s2, 0
	s_lshl_b32 s2, s18, 2
	s_add_i32 s37, s2, s8
	s_waitcnt lgkmcnt(0)
	s_lshl_b32 s2, s6, 2
	s_add_i32 s2, s2, 4
	s_and_b32 s38, s2, -8
	s_cmpk_lt_i32 s37, 0x1400
	s_cselect_b64 s[2:3], -1, 0
	s_add_u32 s39, s4, 0x2000000
	s_addc_u32 s40, s5, 0
	s_lshl_b32 s4, s18, 3
	s_add_i32 s57, s8, s4
	s_lshl_b32 s41, s6, 3
	s_addk_i32 s57, 0x1400
	s_movk_i32 s32, 0x4c00
	s_cmpk_eq_i32 s99, 0x100
	s_cselect_b32 s32, 0x3800, s32
	s_cmp_lt_i32 s57, s32
	s_cselect_b64 s[14:15], -1, 0
	s_lshl_b32 s4, s50, 3
	s_bfe_u32 s6, s61, 0x20006
	s_lshr_b32 s7, s61, 8
	s_add_i32 s59, s8, s4
	s_add_i32 s5, s41, 0x2fff
	s_mov_b32 s20, s61
	s_lshl_b32 s61, s8, 10
	s_lshl_b32 s63, s7, 6
	s_lshl_b32 s65, s7, 13
	s_lshl_b32 s67, s6, 12
	s_cmpk_lt_i32 s18, 0x600
	s_cselect_b64 s[16:17], -1, 0
	s_ashr_i32 s4, s18, 31
	s_lshr_b32 s4, s4, 29
	s_add_i32 s4, s18, s4
	s_ashr_i32 s8, s4, 3
	s_and_b32 s4, s4, -8
	s_sub_i32 s4, s18, s4
	s_cmp_lt_i32 s4, 0
	s_movk_i32 s69, 0xc1
	s_cselect_b32 s18, s69, 0xc0
	s_mul_i32 s4, s18, s4
	s_add_i32 s4, s4, s8
	s_mul_hi_i32 s8, s4, 0x2aaaaaab
	s_lshr_b32 s18, s8, 31
	s_ashr_i32 s8, s8, 4
	s_add_i32 s8, s8, s18
	s_lshl_b32 s82, s8, 3
	s_mulk_i32 s8, 0x60
	s_sub_i32 s8, s4, s8
	s_bfe_i32 s4, s8, 0x80000
	s_bfe_u32 s4, s4, 0x3000c
	s_add_i32 s18, s8, s4
	s_bfe_i32 s4, s18, 0x80000
	s_and_b32 s18, s18, 0xf8
	s_sub_i32 s8, s8, s18
	s_sext_i32_i16 s19, s4
	s_sext_i32_i8 s8, s8
	s_lshr_b32 s4, s19, 3
	s_add_i32 s82, s82, s8
	s_ashr_i32 s44, s19, 3
	s_cmp_eq_u32 s7, 1
	s_cselect_b64 s[18:19], -1, 0
	s_cmpk_lt_u32 s20, 0x100
	s_cselect_b64 s[20:21], -1, 0
	s_and_b64 s[22:23], s[0:1], s[2:3]
	s_abs_i32 s2, s41
	v_cvt_f32_u32_e32 v0, s2
	s_bfe_i64 s[0:1], s[4:5], 0x100000
	s_sub_i32 s3, 0, s2
	s_lshl_b64 s[26:27], s[0:1], 20
	v_rcp_iflag_f32_e32 v0, v0
	s_abs_i32 s1, s5
	s_lshl_b32 s86, s82, 8
	s_xor_b32 s0, s5, s41
	v_mul_f32_e32 v0, 0x4f7ffffe, v0
	v_cvt_u32_f32_e32 v0, v0
	s_lshl_b32 s84, s6, 6
	s_lshl_b32 s85, s82, 20
	s_bitset1_b32 s86, 7
	v_readfirstlane_b32 s4, v0
	s_mul_i32 s3, s3, s4
	s_mul_hi_u32 s3, s4, s3
	s_add_i32 s4, s4, s3
	s_mul_hi_u32 s3, s1, s4
	s_mul_i32 s4, s3, s2
	s_sub_i32 s1, s1, s4
	s_ashr_i32 s0, s0, 31
	s_add_i32 s4, s3, 1
	s_sub_i32 s5, s1, s2
	s_cmp_ge_u32 s1, s2
	s_cselect_b32 s3, s4, s3
	s_cselect_b32 s1, s5, s1
	s_add_i32 s4, s3, 1
	s_cmp_ge_u32 s1, s2
	s_cselect_b32 s1, s4, s3
	s_xor_b32 s1, s1, s0
	s_sub_i32 s87, s1, s0
	s_mov_b32 s9, 0
	s_mov_b64 s[12:13], 0x2000000
	s_add_i32 s88, s87, -1
	v_mov_b32_e32 v161, 0
	s_movk_i32 s89, 0x104
	s_movk_i32 s90, 0x4000
	s_mov_b32 s91, 0x8000
	s_mov_b32 s92, 0xc000
	s_mov_b32 s93, 0x10000
	s_mov_b64 s[52:53], 0x80
	s_mov_b64 s[54:55], 0x32000080
	s_mov_b32 s56, 0x3e6d3388
	s_mov_b32 s58, 0x3f07dc22
	s_mov_b32 s60, 0xbf3a00e3
	s_mov_b32 s62, 0x3f35f0e3
	s_mov_b32 s64, 0xbe11a98e
	s_mov_b32 s66, 0x3e027906
	s_mov_b32 s68, 0xbf38aa3b
	s_movk_i32 s94, 0x1800
	s_mov_b32 s95, 0x2001000
	v_mov_b32_e32 v176, 1
	s_mov_b32 s96, 0
	s_branch .LBB0_218

.LBB0_227:
	s_lshl_b32 s3, s4, 6
	s_lshr_b32 s5, s4, 3
	s_ashr_i32 s2, s4, 10
	s_cmpk_eq_i32 s99, 0x100
	s_cselect_b32 s32, 12, 0x7fff
	s_cmp_ge_i32 s2, s32
	s_cselect_b32 s32, 2, 0
	s_add_i32 s2, s2, s32
	s_and_b32 s3, s3, 0xfc0
	s_and_b32 s5, s5, 8
	s_or_b32 s5, s5, s3
	s_ashr_i32 s3, s2, 31
	s_lshl_b64 s[6:7], s[2:3], 25
	s_waitcnt lgkmcnt(0)
	s_add_u32 s6, s0, s6
	s_addc_u32 s7, s1, s7
	s_lshl_b32 s8, s4, 1
	s_and_b32 s8, s8, 0x700
	s_lshl_b32 s24, s8, 14
	s_add_u32 s6, s6, s24
	s_addc_u32 s7, s7, 0
	s_lshl_b32 s24, s4, 7
	s_and_b32 s24, s24, 0x3f80
	s_add_u32 s6, s6, s24
	s_addc_u32 s7, s7, 0
	v_lshl_add_u64 v[0:1], s[6:7], 0, v[160:161]
	v_lshl_add_u64 v[32:33], v[0:1], 0, v[2:3]
	v_add_co_u32_e32 v28, vcc, s90, v32
	v_lshl_add_u64 v[52:53], v[0:1], 0, v[4:5]
	s_nop 0
	v_addc_co_u32_e32 v29, vcc, 0, v33, vcc
	global_load_dwordx4 v[22:25], v[32:33], off nt
	s_nop 0
	global_load_dwordx4 v[28:31], v[28:29], off nt
	v_add_co_u32_e32 v34, vcc, s91, v32
	v_lshl_add_u64 v[56:57], v[0:1], 0, v[6:7]
	s_nop 0
	v_addc_co_u32_e32 v35, vcc, 0, v33, vcc
	v_add_co_u32_e32 v36, vcc, s92, v32
	v_mov_b32_e32 v27, v161
	s_nop 0
	v_addc_co_u32_e32 v37, vcc, 0, v33, vcc
	global_load_dwordx4 v[32:35], v[34:35], off nt
	s_nop 0
	global_load_dwordx4 v[36:39], v[36:37], off nt
	v_add_co_u32_e32 v44, vcc, s90, v52
	v_mov_b32_e32 v72, v161
	s_nop 0
	v_addc_co_u32_e32 v45, vcc, 0, v53, vcc
	global_load_dwordx4 v[40:43], v[52:53], off nt
	s_nop 0
	global_load_dwordx4 v[44:47], v[44:45], off nt
	v_add_co_u32_e32 v48, vcc, s91, v52
	v_mov_b32_e32 v73, v161
	s_nop 0
	v_addc_co_u32_e32 v49, vcc, 0, v53, vcc
	v_add_co_u32_e32 v52, vcc, s92, v52
	global_load_dwordx4 v[48:51], v[48:49], off nt
	s_nop 0
	v_addc_co_u32_e32 v53, vcc, 0, v53, vcc
	global_load_dwordx4 v[52:55], v[52:53], off nt
	v_add_co_u32_e32 v60, vcc, s90, v56
	v_mov_b32_e32 v74, v161
	s_nop 0
	v_addc_co_u32_e32 v61, vcc, 0, v57, vcc
	v_add_co_u32_e32 v64, vcc, s91, v56
	v_mov_b32_e32 v75, v161
	s_nop 0
	v_addc_co_u32_e32 v65, vcc, 0, v57, vcc
	v_add_co_u32_e32 v68, vcc, s92, v56
	v_mov_b32_e32 v88, v161
	s_nop 0
	v_addc_co_u32_e32 v69, vcc, 0, v57, vcc
	global_load_dwordx4 v[56:59], v[56:57], off nt
	s_nop 0
	global_load_dwordx4 v[60:63], v[60:61], off nt
	s_nop 0
	global_load_dwordx4 v[64:67], v[64:65], off nt
	s_nop 0
	global_load_dwordx4 v[68:71], v[68:69], off nt
	s_lshl_b64 s[2:3], s[2:3], 23
	s_lshl_b32 s5, s5, 11
	s_add_u32 s2, s39, s2
	s_addc_u32 s3, s40, s3
	s_add_u32 s2, s2, s5
	s_addc_u32 s3, s3, 0
	s_add_u32 s2, s2, s8
	s_addc_u32 s3, s3, 0
	s_waitcnt vmcnt(11)
	v_mul_f32_e32 v22, 0x43800000, v22
	v_mul_f32_e32 v23, 0x43800000, v23
	s_waitcnt vmcnt(10)
	v_mul_f32_e32 v28, 0x43800000, v28
	v_mul_f32_e32 v29, 0x43800000, v29
	v_cvt_pk_fp8_f32 v27, v22, v28
	v_cvt_pk_fp8_f32 v72, v23, v29
	v_mul_f32_e32 v24, 0x43800000, v24
	v_mul_f32_e32 v25, 0x43800000, v25
	v_mul_f32_e32 v30, 0x43800000, v30
	v_mul_f32_e32 v22, 0x43800000, v31
	v_cvt_pk_fp8_f32 v73, v24, v30
	s_waitcnt vmcnt(9)
	v_mul_f32_e32 v32, 0x43800000, v32
	s_waitcnt vmcnt(8)
	v_mul_f32_e32 v36, 0x43800000, v36
	v_mul_f32_e32 v33, 0x43800000, v33
	v_mul_f32_e32 v37, 0x43800000, v37
	v_cvt_pk_fp8_f32 v74, v25, v22
	v_cvt_pk_fp8_f32 v27, v32, v36 op_sel:[0,0,1]
	v_cvt_pk_fp8_f32 v72, v33, v37 op_sel:[0,0,1]
	v_lshl_add_u64 v[32:33], v[0:1], 0, v[8:9]
	v_add_co_u32_e32 v28, vcc, s90, v32
	v_mul_f32_e32 v34, 0x43800000, v34
	v_mul_f32_e32 v38, 0x43800000, v38
	v_mul_f32_e32 v22, 0x43800000, v35
	v_mul_f32_e32 v23, 0x43800000, v39
	v_addc_co_u32_e32 v29, vcc, 0, v33, vcc
	v_cvt_pk_fp8_f32 v73, v34, v38 op_sel:[0,0,1]
	v_cvt_pk_fp8_f32 v74, v22, v23 op_sel:[0,0,1]
	global_load_dwordx4 v[22:25], v[32:33], off nt
	s_nop 0
	global_load_dwordx4 v[28:31], v[28:29], off nt
	v_add_co_u32_e32 v34, vcc, s91, v32
	s_waitcnt vmcnt(9)
	v_mul_f32_e32 v40, 0x43800000, v40
	v_addc_co_u32_e32 v35, vcc, 0, v33, vcc
	v_add_co_u32_e32 v36, vcc, s92, v32
	s_waitcnt vmcnt(8)
	v_mul_f32_e32 v44, 0x43800000, v44
	v_addc_co_u32_e32 v37, vcc, 0, v33, vcc
	global_load_dwordx4 v[32:35], v[34:35], off nt
	s_nop 0
	global_load_dwordx4 v[36:39], v[36:37], off nt
	v_cvt_pk_fp8_f32 v75, v40, v44
	v_mul_f32_e32 v40, 0x43800000, v41
	v_mul_f32_e32 v41, 0x43800000, v45
	v_mov_b32_e32 v44, v161
	v_cvt_pk_fp8_f32 v44, v40, v41
	s_waitcnt vmcnt(9)
	v_mul_f32_e32 v40, 0x43800000, v49
	s_waitcnt vmcnt(8)
	v_mul_f32_e32 v41, 0x43800000, v53
	v_mul_f32_e32 v48, 0x43800000, v48
	v_cvt_pk_fp8_f32 v44, v40, v41 op_sel:[0,0,1]
	v_mul_f32_e32 v40, 0x43800000, v42
	v_mul_f32_e32 v41, 0x43800000, v46
	v_mov_b32_e32 v46, v161
	v_cvt_pk_fp8_f32 v46, v40, v41
	v_mul_f32_e32 v40, 0x43800000, v43
	v_mul_f32_e32 v41, 0x43800000, v47
	v_mov_b32_e32 v43, v161
	v_mul_f32_e32 v52, 0x43800000, v52
	v_cvt_pk_fp8_f32 v43, v40, v41
	v_cvt_pk_fp8_f32 v75, v48, v52 op_sel:[0,0,1]
	v_mul_f32_e32 v42, 0x43800000, v50
	v_mul_f32_e32 v45, 0x43800000, v54
	v_cvt_pk_fp8_f32 v46, v42, v45 op_sel:[0,0,1]
	v_mul_f32_e32 v40, 0x43800000, v51
	v_mul_f32_e32 v41, 0x43800000, v55
	v_cvt_pk_fp8_f32 v43, v40, v41 op_sel:[0,0,1]
	ds_write2_b32 v19, v27, v75 offset1:8
	ds_write2_b32 v19, v72, v44 offset0:65 offset1:73
	ds_write2_b32 v19, v73, v46 offset0:130 offset1:138
	ds_write2_b32 v19, v74, v43 offset0:195 offset1:203
	s_waitcnt vmcnt(7)
	v_mul_f32_e32 v27, 0x43800000, v56
	s_waitcnt vmcnt(6)
	v_mul_f32_e32 v40, 0x43800000, v60
	v_mov_b32_e32 v56, v161
	v_cvt_pk_fp8_f32 v56, v27, v40
	v_mul_f32_e32 v27, 0x43800000, v57
	v_mul_f32_e32 v52, 0x43800000, v61
	v_mov_b32_e32 v72, v161
	v_cvt_pk_fp8_f32 v72, v27, v52
	s_waitcnt vmcnt(5)
	v_mul_f32_e32 v50, 0x43800000, v64
	s_waitcnt vmcnt(4)
	v_mul_f32_e32 v51, 0x43800000, v68
	v_lshl_add_u64 v[48:49], v[0:1], 0, v[10:11]
	v_add_co_u32_e32 v44, vcc, s90, v48
	v_cvt_pk_fp8_f32 v56, v50, v51 op_sel:[0,0,1]
	v_mul_f32_e32 v27, 0x43800000, v65
	v_mul_f32_e32 v50, 0x43800000, v69
	v_addc_co_u32_e32 v45, vcc, 0, v49, vcc
	v_cvt_pk_fp8_f32 v72, v27, v50 op_sel:[0,0,1]
	v_mul_f32_e32 v27, 0x43800000, v58
	v_mul_f32_e32 v50, 0x43800000, v62
	v_mov_b32_e32 v73, v161
	global_load_dwordx4 v[40:43], v[48:49], off nt
	s_nop 0
	global_load_dwordx4 v[44:47], v[44:45], off nt
	v_cvt_pk_fp8_f32 v73, v27, v50
	v_add_co_u32_e32 v50, vcc, s91, v48
	v_mul_f32_e32 v57, 0x43800000, v66
	s_nop 0
	v_addc_co_u32_e32 v51, vcc, 0, v49, vcc
	v_add_co_u32_e32 v52, vcc, s92, v48
	v_mul_f32_e32 v58, 0x43800000, v70
	s_nop 0
	v_addc_co_u32_e32 v53, vcc, 0, v49, vcc
	global_load_dwordx4 v[48:51], v[50:51], off nt
	s_nop 0
	global_load_dwordx4 v[52:55], v[52:53], off nt
	v_cvt_pk_fp8_f32 v73, v57, v58 op_sel:[0,0,1]
	v_mul_f32_e32 v27, 0x43800000, v59
	v_mul_f32_e32 v57, 0x43800000, v63
	v_mov_b32_e32 v74, v161
	v_cvt_pk_fp8_f32 v74, v27, v57
	v_mul_f32_e32 v58, 0x43800000, v67
	s_waitcnt vmcnt(7)
	v_mul_f32_e32 v22, 0x43800000, v22
	s_waitcnt vmcnt(6)
	v_mul_f32_e32 v27, 0x43800000, v28
	v_mov_b32_e32 v28, v161
	v_cvt_pk_fp8_f32 v28, v22, v27
	v_mul_f32_e32 v59, 0x43800000, v71
	v_cvt_pk_fp8_f32 v74, v58, v59 op_sel:[0,0,1]
	v_mul_f32_e32 v24, 0x43800000, v24
	v_mul_f32_e32 v30, 0x43800000, v30
	s_waitcnt vmcnt(5)
	v_mul_f32_e32 v22, 0x43800000, v32
	s_waitcnt vmcnt(4)
	v_mul_f32_e32 v27, 0x43800000, v36
	v_cvt_pk_fp8_f32 v28, v22, v27 op_sel:[0,0,1]
	v_mul_f32_e32 v22, 0x43800000, v23
	v_mul_f32_e32 v23, 0x43800000, v29
	v_mov_b32_e32 v27, v161
	v_cvt_pk_fp8_f32 v27, v22, v23
	v_mul_f32_e32 v22, 0x43800000, v33
	v_mul_f32_e32 v23, 0x43800000, v37
	ds_write2_b32 v19, v56, v28 offset0:16 offset1:24
	v_cvt_pk_fp8_f32 v27, v22, v23 op_sel:[0,0,1]
	v_lshl_add_u64 v[22:23], v[0:1], 0, v[12:13]
	v_add_co_u32_e32 v28, vcc, s90, v22
	v_mov_b32_e32 v32, v161
	s_nop 0
	v_addc_co_u32_e32 v29, vcc, 0, v23, vcc
	global_load_dwordx4 v[56:59], v[22:23], off nt
	global_load_dwordx4 v[60:63], v[28:29], off nt
	v_add_co_u32_e32 v28, vcc, s91, v22
	v_cvt_pk_fp8_f32 v32, v24, v30
	s_nop 0
	v_addc_co_u32_e32 v29, vcc, 0, v23, vcc
	v_add_co_u32_e32 v22, vcc, s92, v22
	s_waitcnt vmcnt(5)
	v_mul_f32_e32 v40, 0x43800000, v40
	v_addc_co_u32_e32 v23, vcc, 0, v23, vcc
	global_load_dwordx4 v[64:67], v[28:29], off nt
	global_load_dwordx4 v[68:71], v[22:23], off nt
	v_mul_f32_e32 v22, 0x43800000, v34
	v_mul_f32_e32 v23, 0x43800000, v38
	v_cvt_pk_fp8_f32 v32, v22, v23 op_sel:[0,0,1]
	ds_write2_b32 v19, v72, v27 offset0:81 offset1:89
	v_mul_f32_e32 v22, 0x43800000, v25
	v_mul_f32_e32 v23, 0x43800000, v31
	v_mov_b32_e32 v27, v161
	v_cvt_pk_fp8_f32 v27, v22, v23
	ds_write2_b32 v19, v73, v32 offset0:146 offset1:154
	v_lshl_add_u64 v[32:33], v[0:1], 0, v[14:15]
	v_add_co_u32_e32 v28, vcc, s90, v32
	v_mul_f32_e32 v22, 0x43800000, v35
	v_mul_f32_e32 v23, 0x43800000, v39
	v_addc_co_u32_e32 v29, vcc, 0, v33, vcc
	v_cvt_pk_fp8_f32 v27, v22, v23 op_sel:[0,0,1]
	global_load_dwordx4 v[22:25], v[32:33], off nt
	s_nop 0
	global_load_dwordx4 v[28:31], v[28:29], off nt
	v_add_co_u32_e32 v34, vcc, s91, v32
	s_waitcnt vmcnt(8)
	v_mul_f32_e32 v44, 0x43800000, v44
	v_addc_co_u32_e32 v35, vcc, 0, v33, vcc
	v_add_co_u32_e32 v36, vcc, s92, v32
	v_cvt_pk_fp8_f32 v88, v40, v44
	s_nop 0
	v_addc_co_u32_e32 v37, vcc, 0, v33, vcc
	global_load_dwordx4 v[32:35], v[34:35], off nt
	s_nop 0
	global_load_dwordx4 v[36:39], v[36:37], off nt
	ds_write2_b32 v19, v74, v27 offset0:211 offset1:219
	s_waitcnt vmcnt(9)
	v_mul_f32_e32 v27, 0x43800000, v48
	s_waitcnt vmcnt(8)
	v_mul_f32_e32 v40, 0x43800000, v52
	v_cvt_pk_fp8_f32 v88, v27, v40 op_sel:[0,0,1]
	v_mul_f32_e32 v27, 0x43800000, v41
	v_mul_f32_e32 v40, 0x43800000, v45
	v_mov_b32_e32 v45, v161
	v_lshl_add_u64 v[0:1], v[0:1], 0, v[16:17]
	v_cvt_pk_fp8_f32 v45, v27, v40
	v_add_co_u32_e32 v40, vcc, s90, v0
	v_mul_f32_e32 v44, 0x43800000, v49
	s_nop 0
	v_addc_co_u32_e32 v41, vcc, 0, v1, vcc
	global_load_dwordx4 v[72:75], v[0:1], off nt
	global_load_dwordx4 v[76:79], v[40:41], off nt
	v_add_co_u32_e32 v40, vcc, s91, v0
	v_mul_f32_e32 v27, 0x43800000, v50
	s_nop 0
	v_addc_co_u32_e32 v41, vcc, 0, v1, vcc
	v_add_co_u32_e32 v0, vcc, s92, v0
	s_nop 1
	v_addc_co_u32_e32 v1, vcc, 0, v1, vcc
	global_load_dwordx4 v[80:83], v[40:41], off nt
	global_load_dwordx4 v[84:87], v[0:1], off nt
	v_mul_f32_e32 v0, 0x43800000, v53
	v_cvt_pk_fp8_f32 v45, v44, v0 op_sel:[0,0,1]
	v_mul_f32_e32 v0, 0x43800000, v42
	v_mul_f32_e32 v1, 0x43800000, v46
	v_mov_b32_e32 v41, v161
	v_cvt_pk_fp8_f32 v41, v0, v1
	v_mul_f32_e32 v0, 0x43800000, v43
	v_mul_f32_e32 v1, 0x43800000, v47
	v_mov_b32_e32 v42, v161
	v_cvt_pk_fp8_f32 v42, v0, v1
	v_mul_f32_e32 v0, 0x43800000, v51
	v_mul_f32_e32 v1, 0x43800000, v55
	v_mov_b32_e32 v43, v161
	v_cvt_pk_fp8_f32 v42, v0, v1 op_sel:[0,0,1]
	s_waitcnt vmcnt(11)
	v_mul_f32_e32 v0, 0x43800000, v56
	s_waitcnt vmcnt(10)
	v_mul_f32_e32 v1, 0x43800000, v60
	v_cvt_pk_fp8_f32 v43, v0, v1
	v_mul_f32_e32 v0, 0x43800000, v57
	v_mul_f32_e32 v1, 0x43800000, v61
	v_mov_b32_e32 v44, v161
	v_cvt_pk_fp8_f32 v44, v0, v1
	v_mov_b32_e32 v46, v161
	v_mov_b32_e32 v47, v161
	s_waitcnt vmcnt(9)
	v_mul_f32_e32 v0, 0x43800000, v65
	s_waitcnt vmcnt(8)
	v_mul_f32_e32 v1, 0x43800000, v69
	v_cvt_pk_fp8_f32 v44, v0, v1 op_sel:[0,0,1]
	v_mul_f32_e32 v0, 0x43800000, v58
	v_mul_f32_e32 v1, 0x43800000, v62
	v_cvt_pk_fp8_f32 v46, v0, v1
	v_mul_f32_e32 v0, 0x43800000, v59
	v_mul_f32_e32 v1, 0x43800000, v63
	v_cvt_pk_fp8_f32 v47, v0, v1
	v_mul_f32_e32 v0, 0x43800000, v67
	v_mul_f32_e32 v1, 0x43800000, v71
	v_mul_f32_e32 v40, 0x43800000, v54
	v_cvt_pk_fp8_f32 v47, v0, v1 op_sel:[0,0,1]
	v_cvt_pk_fp8_f32 v41, v27, v40 op_sel:[0,0,1]
	v_mul_f32_e32 v27, 0x43800000, v64
	v_mul_f32_e32 v40, 0x43800000, v68
	v_cvt_pk_fp8_f32 v43, v27, v40 op_sel:[0,0,1]
	v_mul_f32_e32 v27, 0x43800000, v66
	s_waitcnt vmcnt(7)
	v_mul_f32_e32 v0, 0x43800000, v22
	s_waitcnt vmcnt(6)
	v_mul_f32_e32 v1, 0x43800000, v28
	v_mov_b32_e32 v28, v161
	v_cvt_pk_fp8_f32 v28, v0, v1
	v_mul_f32_e32 v0, 0x43800000, v23
	v_mul_f32_e32 v1, 0x43800000, v29
	v_mov_b32_e32 v23, v161
	v_cvt_pk_fp8_f32 v23, v0, v1
	v_mul_f32_e32 v40, 0x43800000, v70
	v_cvt_pk_fp8_f32 v46, v27, v40 op_sel:[0,0,1]
	v_mov_b32_e32 v29, v161
	s_waitcnt vmcnt(5)
	v_mul_f32_e32 v22, 0x43800000, v32
	s_waitcnt vmcnt(4)
	v_mul_f32_e32 v27, 0x43800000, v36
	v_mul_f32_e32 v0, 0x43800000, v33
	v_mul_f32_e32 v1, 0x43800000, v37
	v_cvt_pk_fp8_f32 v28, v22, v27 op_sel:[0,0,1]
	v_cvt_pk_fp8_f32 v23, v0, v1 op_sel:[0,0,1]
	v_mul_f32_e32 v0, 0x43800000, v24
	v_mul_f32_e32 v1, 0x43800000, v30
	v_mov_b32_e32 v27, v161
	v_cvt_pk_fp8_f32 v27, v0, v1
	v_mul_f32_e32 v0, 0x43800000, v25
	v_mul_f32_e32 v1, 0x43800000, v31
	v_mov_b32_e32 v25, v161
	v_cvt_pk_fp8_f32 v25, v0, v1
	v_mul_f32_e32 v0, 0x43800000, v35
	v_mul_f32_e32 v1, 0x43800000, v39
	v_mov_b32_e32 v30, v161
	v_cvt_pk_fp8_f32 v25, v0, v1 op_sel:[0,0,1]
	s_waitcnt vmcnt(3)
	v_mul_f32_e32 v0, 0x43800000, v72
	s_waitcnt vmcnt(2)
	v_mul_f32_e32 v1, 0x43800000, v76
	v_cvt_pk_fp8_f32 v29, v0, v1
	v_mul_f32_e32 v0, 0x43800000, v73
	v_mul_f32_e32 v1, 0x43800000, v77
	v_cvt_pk_fp8_f32 v30, v0, v1
	v_mov_b32_e32 v31, v161
	v_mul_f32_e32 v22, 0x43800000, v34
	s_waitcnt vmcnt(1)
	v_mul_f32_e32 v0, 0x43800000, v81
	s_waitcnt vmcnt(0)
	v_mul_f32_e32 v1, 0x43800000, v85
	v_cvt_pk_fp8_f32 v30, v0, v1 op_sel:[0,0,1]
	v_mul_f32_e32 v0, 0x43800000, v74
	v_mul_f32_e32 v1, 0x43800000, v78
	v_mul_f32_e32 v24, 0x43800000, v38
	v_cvt_pk_fp8_f32 v31, v0, v1
	v_mul_f32_e32 v0, 0x43800000, v75
	v_mul_f32_e32 v1, 0x43800000, v79
	v_mov_b32_e32 v32, v161
	v_cvt_pk_fp8_f32 v27, v22, v24 op_sel:[0,0,1]
	v_mul_f32_e32 v22, 0x43800000, v80
	v_mul_f32_e32 v24, 0x43800000, v84
	v_cvt_pk_fp8_f32 v32, v0, v1
	v_cvt_pk_fp8_f32 v29, v22, v24 op_sel:[0,0,1]
	v_mul_f32_e32 v22, 0x43800000, v82
	v_mul_f32_e32 v24, 0x43800000, v86
	v_cvt_pk_fp8_f32 v31, v22, v24 op_sel:[0,0,1]
	v_mul_f32_e32 v0, 0x43800000, v83
	v_mul_f32_e32 v1, 0x43800000, v87
	v_cvt_pk_fp8_f32 v32, v0, v1 op_sel:[0,0,1]
	ds_write2_b32 v19, v88, v43 offset0:32 offset1:40
	ds_write2_b32 v19, v45, v44 offset0:97 offset1:105
	ds_write2_b32 v19, v41, v46 offset0:162 offset1:170
	ds_write2_b32 v19, v42, v47 offset0:227 offset1:235
	ds_write2_b32 v19, v28, v29 offset0:48 offset1:56
	ds_write2_b32 v19, v23, v30 offset0:113 offset1:121
	ds_write2_b32 v19, v27, v31 offset0:178 offset1:186
	ds_write2_b32 v19, v25, v32 offset0:243 offset1:251
	s_waitcnt lgkmcnt(0)
	v_lshl_add_u64 v[0:1], s[2:3], 0, v[20:21]
	s_mov_b32 s2, 0
.LBB0_228:
	v_add_u32_e32 v22, s2, v26
	v_ashrrev_i32_e32 v23, 4, v22
	v_ashrrev_i32_e32 v27, 3, v22
	v_add_u32_e32 v28, 64, v22
	v_add_u32_e32 v29, 0x80, v22
	v_add_u32_e32 v22, 0xc0, v22
	v_and_b32_e32 v30, 7, v23
	v_ashrrev_i32_e32 v32, 4, v28
	v_ashrrev_i32_e32 v33, 3, v28
	v_ashrrev_i32_e32 v28, 4, v29
	v_ashrrev_i32_e32 v36, 3, v29
	v_ashrrev_i32_e32 v29, 4, v22
	v_mad_u64_u32 v[24:25], s[6:7], v23, s89, v[18:19]
	v_and_or_b32 v40, v27, -16, v30
	v_mad_u64_u32 v[30:31], s[6:7], v32, s89, v[18:19]
	v_and_b32_e32 v27, 7, v32
	v_mad_u64_u32 v[34:35], s[6:7], v28, s89, v[18:19]
	v_and_b32_e32 v32, 7, v28
	v_mad_u64_u32 v[38:39], s[6:7], v29, s89, v[18:19]
	v_ashrrev_i32_e32 v43, 3, v22
	ds_read2_b32 v[22:23], v24 offset1:1
	ds_read2_b32 v[24:25], v24 offset0:2 offset1:3
	v_and_b32_e32 v45, 7, v29
	ds_read2_b32 v[28:29], v30 offset1:1
	ds_read2_b32 v[30:31], v30 offset0:2 offset1:3
	v_and_or_b32 v42, v33, -16, v27
	v_and_or_b32 v44, v36, -16, v32
	ds_read2_b32 v[32:33], v34 offset1:1
	ds_read2_b32 v[34:35], v34 offset0:2 offset1:3
	ds_read2_b32 v[36:37], v38 offset1:1
	ds_read2_b32 v[38:39], v38 offset0:2 offset1:3
	v_ashrrev_i32_e32 v41, 31, v40
	v_and_or_b32 v46, v43, -16, v45
	s_addk_i32 s2, 0x100
	v_lshlrev_b64 v[40:41], 11, v[40:41]
	v_ashrrev_i32_e32 v43, 31, v42
	v_ashrrev_i32_e32 v45, 31, v44
	v_ashrrev_i32_e32 v47, 31, v46
	s_cmpk_lg_i32 s2, 0x200
	v_lshl_add_u64 v[40:41], v[0:1], 0, v[40:41]
	v_lshlrev_b64 v[42:43], 11, v[42:43]
	v_lshlrev_b64 v[44:45], 11, v[44:45]
	v_lshlrev_b64 v[46:47], 11, v[46:47]
	v_lshl_add_u64 v[42:43], v[0:1], 0, v[42:43]
	v_lshl_add_u64 v[44:45], v[0:1], 0, v[44:45]
	v_lshl_add_u64 v[46:47], v[0:1], 0, v[46:47]
	s_waitcnt lgkmcnt(6)
	global_store_dwordx4 v[40:41], v[22:25], off
	s_waitcnt lgkmcnt(4)
	global_store_dwordx4 v[42:43], v[28:31], off
	s_waitcnt lgkmcnt(2)
	global_store_dwordx4 v[44:45], v[32:35], off
	s_waitcnt lgkmcnt(0)
	global_store_dwordx4 v[46:47], v[36:39], off
	s_cbranch_scc1 .LBB0_228
	s_waitcnt lgkmcnt(0)
	s_add_i32 s4, s4, s41
	s_movk_i32 s32, 0x4c00
	s_cmpk_eq_i32 s99, 0x100
	s_cselect_b32 s32, 0x3800, s32
	s_cmp_lt_i32 s4, s32
	s_cbranch_scc1 .LBB0_227

.LBB0_729:
	s_ashr_i32 s26, s52, 12
	s_add_i32 s46, s26, 28
	s_ashr_i32 s47, s46, 31
	s_lshl_b64 s[26:27], s[46:47], 25
	s_add_u32 s26, s30, s26
	s_addc_u32 s27, s31, s27
	s_lshr_b32 s40, s52, 1
	s_and_b32 s40, s40, 0x7c0
	v_add_lshl_u32 v32, s40, v76, 12
	s_and_b32 s48, s53, 0xfe0
	v_or3_b32 v82, v32, v160, s48
	v_lshl_add_u64 v[56:57], v[82:83], 2, s[26:27]
	s_cmpk_lg_i32 s99, 0x100
	s_cbranch_scc1 .Lp5dbl_noissue
	s_cmp_gt_u32 s77, 3
	s_cbranch_scc1 .Lp5dbl_noissue
	s_sub_u32 vcc_lo, s26, 0x20000000
	s_subb_u32 vcc_hi, s27, 0
	v_lshlrev_b32_e32 v226, 2, v82
	v_add_u32_e32 v230, s64, v226
	v_add_u32_e32 v234, s65, v226
	v_add_u32_e32 v238, s66, v226
	v_add_u32_e32 v242, s67, v226
	v_add_u32_e32 v246, s68, v226
	v_add_u32_e32 v250, s69, v226
	v_add_u32_e32 v178, s70, v226
	global_load_dwordx4 v[226:229], v226, vcc nt
	global_load_dwordx4 v[230:233], v230, vcc nt
	global_load_dwordx4 v[234:237], v234, vcc nt
	global_load_dwordx4 v[238:241], v238, vcc nt
	global_load_dwordx4 v[242:245], v242, vcc nt
	global_load_dwordx4 v[246:249], v246, vcc nt
	global_load_dwordx4 v[250:253], v250, vcc nt
	global_load_dwordx4 v[178:181], v178, vcc nt

.LBB0_734:
	v_mul_f32_e32 v32, 0x43800000, v32
	v_mul_f32_e32 v36, 0x43800000, v36
	v_mov_b32_e32 v66, v83
	v_cvt_pk_fp8_f32 v66, v32, v36
	v_mul_f32_e32 v32, 0x43800000, v48
	v_mul_f32_e32 v36, 0x43800000, v52
	v_mov_b32_e32 v67, v83
	v_cvt_pk_fp8_f32 v67, v32, v36
	v_mul_f32_e32 v32, 0x43800000, v56
	v_mul_f32_e32 v36, 0x43800000, v60
	s_lshr_b32 s26, s53, 8
	v_cvt_pk_fp8_f32 v67, v32, v36 op_sel:[0,0,1]
	v_mul_f32_e32 v33, 0x43800000, v33
	v_mul_f32_e32 v36, 0x43800000, v37
	v_mov_b32_e32 v32, v83
	s_and_b32 s26, s26, 8
	v_mul_f32_e32 v37, 0x43800000, v41
	v_cvt_pk_fp8_f32 v32, v33, v36
	v_mul_f32_e32 v36, 0x43800000, v49
	v_mul_f32_e32 v41, 0x43800000, v53
	v_mov_b32_e32 v33, v83
	s_or_b32 s48, s50, s26
	s_lshl_b64 s[26:27], s[46:47], 12
	v_cvt_pk_fp8_f32 v33, v36, v41
	s_or_b32 s26, s26, s48
	v_mul_f32_e32 v40, 0x43800000, v40
	v_mul_f32_e32 v44, 0x43800000, v44
	s_waitcnt lgkmcnt(0)
	v_mov_b32_e32 v65, s27
	v_or_b32_e32 v64, s26, v80
	v_cvt_pk_fp8_f32 v66, v40, v44 op_sel:[0,0,1]
	v_mul_f32_e32 v40, 0x43800000, v45
	v_lshlrev_b64 v[64:65], 11, v[64:65]
	v_cvt_pk_fp8_f32 v32, v37, v40 op_sel:[0,0,1]
	v_mul_f32_e32 v36, 0x43800000, v57
	v_mul_f32_e32 v37, 0x43800000, v61
	v_lshl_add_u64 v[64:65], s[28:29], 0, v[64:65]
	v_cvt_pk_fp8_f32 v33, v36, v37 op_sel:[0,0,1]
	v_lshl_add_u64 v[36:37], v[64:65], 0, s[40:41]
	v_lshl_add_u64 v[36:37], v[36:37], 0, v[76:77]
	global_store_dwordx2 v[36:37], v[66:67], off
	global_store_dwordx2 v[36:37], v[32:33], off offset:2048
	v_mul_f32_e32 v33, 0x43800000, v34
	v_mul_f32_e32 v34, 0x43800000, v38
	v_mov_b32_e32 v32, v83
	v_cvt_pk_fp8_f32 v32, v33, v34
	v_mul_f32_e32 v34, 0x43800000, v50
	v_mul_f32_e32 v41, 0x43800000, v54
	v_mov_b32_e32 v33, v83
	v_cvt_pk_fp8_f32 v33, v34, v41
	v_mul_f32_e32 v38, 0x43800000, v42
	v_mul_f32_e32 v40, 0x43800000, v46
	v_cvt_pk_fp8_f32 v32, v38, v40 op_sel:[0,0,1]
	v_mul_f32_e32 v34, 0x43800000, v58
	v_mul_f32_e32 v38, 0x43800000, v62
	v_cvt_pk_fp8_f32 v33, v34, v38 op_sel:[0,0,1]
	v_mul_f32_e32 v35, 0x43800000, v35
	v_mul_f32_e32 v38, 0x43800000, v39
	v_mov_b32_e32 v34, v83
	v_cvt_pk_fp8_f32 v34, v35, v38
	v_mul_f32_e32 v38, 0x43800000, v51
	v_mul_f32_e32 v41, 0x43800000, v55
	v_mov_b32_e32 v35, v83
	v_cvt_pk_fp8_f32 v35, v38, v41
	v_mul_f32_e32 v39, 0x43800000, v43
	v_mul_f32_e32 v40, 0x43800000, v47
	v_cvt_pk_fp8_f32 v34, v39, v40 op_sel:[0,0,1]
	v_mul_f32_e32 v38, 0x43800000, v59
	v_mul_f32_e32 v39, 0x43800000, v63
	v_cvt_pk_fp8_f32 v35, v38, v39 op_sel:[0,0,1]
	v_add_co_u32_e32 v36, vcc, s72, v36
	v_add_u32_e32 v38, s49, v164
	s_nop 0
	v_addc_co_u32_e32 v37, vcc, 0, v37, vcc
	global_store_dwordx2 v[36:37], v[32:33], off
	global_store_dwordx2 v[36:37], v[34:35], off offset:2048
	s_cmpk_lg_i32 s99, 0x100
	s_cbranch_scc1 .Lp5dbl_noconsume
	s_cmp_gt_u32 s77, 3
	s_cbranch_scc1 .Lp5dbl_noconsume
	s_sub_i32 s46, s46, 16
	v_mul_f32_e32 v226, 0x43800000, v226
	v_mul_f32_e32 v230, 0x43800000, v230
	v_mov_b32_e32 v66, v83
	v_cvt_pk_fp8_f32 v66, v226, v230
	v_mul_f32_e32 v226, 0x43800000, v242
	v_mul_f32_e32 v230, 0x43800000, v246
	v_mov_b32_e32 v67, v83
	v_cvt_pk_fp8_f32 v67, v226, v230
	v_mul_f32_e32 v226, 0x43800000, v250
	v_mul_f32_e32 v230, 0x43800000, v178
	s_lshr_b32 s26, s53, 8
	v_cvt_pk_fp8_f32 v67, v226, v230 op_sel:[0,0,1]
	v_mul_f32_e32 v227, 0x43800000, v227
	v_mul_f32_e32 v230, 0x43800000, v231
	v_mov_b32_e32 v226, v83
	s_and_b32 s26, s26, 8
	v_mul_f32_e32 v231, 0x43800000, v235
	v_cvt_pk_fp8_f32 v226, v227, v230
	v_mul_f32_e32 v230, 0x43800000, v243
	v_mul_f32_e32 v235, 0x43800000, v247
	v_mov_b32_e32 v227, v83
	s_or_b32 s48, s50, s26
	s_lshl_b64 s[26:27], s[46:47], 12
	v_cvt_pk_fp8_f32 v227, v230, v235
	s_or_b32 s26, s26, s48
	v_mul_f32_e32 v234, 0x43800000, v234
	v_mul_f32_e32 v238, 0x43800000, v238
	s_waitcnt lgkmcnt(0)
	v_mov_b32_e32 v65, s27
	v_or_b32_e32 v64, s26, v80
	v_cvt_pk_fp8_f32 v66, v234, v238 op_sel:[0,0,1]
	v_mul_f32_e32 v234, 0x43800000, v239
	v_lshlrev_b64 v[64:65], 11, v[64:65]
	v_cvt_pk_fp8_f32 v226, v231, v234 op_sel:[0,0,1]
	v_mul_f32_e32 v230, 0x43800000, v251
	v_mul_f32_e32 v231, 0x43800000, v179
	v_lshl_add_u64 v[64:65], s[28:29], 0, v[64:65]
	v_cvt_pk_fp8_f32 v227, v230, v231 op_sel:[0,0,1]
	v_lshl_add_u64 v[230:231], v[64:65], 0, s[40:41]
	v_lshl_add_u64 v[230:231], v[230:231], 0, v[76:77]
	global_store_dwordx2 v[230:231], v[66:67], off
	global_store_dwordx2 v[230:231], v[226:227], off offset:2048
	v_mul_f32_e32 v227, 0x43800000, v228
	v_mul_f32_e32 v228, 0x43800000, v232
	v_mov_b32_e32 v226, v83
	v_cvt_pk_fp8_f32 v226, v227, v228
	v_mul_f32_e32 v228, 0x43800000, v244
	v_mul_f32_e32 v235, 0x43800000, v248
	v_mov_b32_e32 v227, v83
	v_cvt_pk_fp8_f32 v227, v228, v235
	v_mul_f32_e32 v232, 0x43800000, v236
	v_mul_f32_e32 v234, 0x43800000, v240
	v_cvt_pk_fp8_f32 v226, v232, v234 op_sel:[0,0,1]
	v_mul_f32_e32 v228, 0x43800000, v252
	v_mul_f32_e32 v232, 0x43800000, v180
	v_cvt_pk_fp8_f32 v227, v228, v232 op_sel:[0,0,1]
	v_mul_f32_e32 v229, 0x43800000, v229
	v_mul_f32_e32 v232, 0x43800000, v233
	v_mov_b32_e32 v228, v83
	v_cvt_pk_fp8_f32 v228, v229, v232
	v_mul_f32_e32 v232, 0x43800000, v245
	v_mul_f32_e32 v235, 0x43800000, v249
	v_mov_b32_e32 v229, v83
	v_cvt_pk_fp8_f32 v229, v232, v235
	v_mul_f32_e32 v233, 0x43800000, v237
	v_mul_f32_e32 v234, 0x43800000, v241
	v_cvt_pk_fp8_f32 v228, v233, v234 op_sel:[0,0,1]
	v_mul_f32_e32 v232, 0x43800000, v253
	v_mul_f32_e32 v233, 0x43800000, v181
	v_cvt_pk_fp8_f32 v229, v232, v233 op_sel:[0,0,1]
	v_add_co_u32_e32 v230, vcc, s72, v230
	v_add_u32_e32 v232, s49, v164
	s_nop 0
	v_addc_co_u32_e32 v231, vcc, 0, v231, vcc
	global_store_dwordx2 v[230:231], v[226:227], off
	global_store_dwordx2 v[230:231], v[228:229], off offset:2048
